# MoE-phase helpers (64) plus 40 proj-phase helpers in layer 0 converting 16384 layer-0 MoE weight items (216 proj workers)
# speedup vs baseline: 1.0298x; 1.0298x over previous
;     ...
;             const int itB = it + NGW;
;             if (itB < NIT) { dB = decode(NIT - 1 - itB); tr_load(dB, vB); }
.Lps_1:
	s_cmp_lt_i32 s44, 0x7e80
	s_cbranch_scc1 .Lpt_1
	s_cmp_ge_i32 s44, 0xbe80
	s_cbranch_scc1 .Lpt_1
	s_add_i32 s44, s44, 0x4000

;     ...
;             const int itA = itB + NGW;
;             if (itA < NIT) { dA = decode(NIT - 1 - itA); tr_load(dA, vA); }
.Lps_2:
	s_cmp_lt_i32 s42, 0x7e80
	s_cbranch_scc1 .Lpt_2
	s_cmp_ge_i32 s42, 0xbe80
	s_cbranch_scc1 .Lpt_2
	s_add_i32 s42, s42, 0x4000

;     ...
;         auto decode = [&](int it) -> TrDesc {
;             TrDesc d; d.zero = 0; d.rope = 0; d.f8 = 0;
;             const int l = it / C_L; int r = it % C_L;
;             const float* W; unsigned char* WT; int ldw, K, k0, n0, scol, esz = 2;
;             if (r < C_IN) { const int kb = r / 188, nb = r % 188; n0 = 64 * nb; k0 = 64 * kb; ldw = NIN; K = D; W = a.w_in + (size_t)l * D * NIN;
;                 if (n0 < 3072) { d.rope = 1; scol = (n0 >> 7) * 128 + 32 * ((n0 >> 6) & 1) + 64 * (q4 >> 3) + 4 * (q4 & 7); }
;                 else if (n0 < 7680) scol = n0 + 4 * q4;
;                 else if (n0 < 11776) scol = n0 + 16 + 4 * q4;
;                 else if (n0 == 11776) { scol = (q4 < 4) ? 7680 + 4 * q4 : 0; d.zero = (q4 < 4) ? 0 : 1; }
;                 else { scol = 0; d.zero = 1; }
;     ...
;                 d.f8 = 1; esz = 1; WT = ws + WS_WIN + (size_t)l * NP * D;
;     ...
;                 WT = ws + WS_WIN + (size_t)l * NP * D * 2;
;     ...
;             } else if ((r -= C_IN) < C_OA) { const int kb = r / 32, nb = r % 32; n0 = 64 * nb; k0 = 64 * kb; ldw = D; K = 512; scol = n0 + 4 * q4; W = a.w_out_a + (size_t)l * 512 * D; WT = ws + WS_WOA + (size_t)l * D * 512 * (MIX_F8 ? 1 : 2); if (MIX_F8) { d.f8 = 1; esz = 1; }
;                 if (BR_FUSE) { K = 1536; WT = ws + WS_WOA + (size_t)l * D * 1536 + 1024; }
;             } else if ((r -= C_OA) < C_OB) { const int kb = r / 32, nb = r % 32; n0 = 64 * nb; k0 = 64 * kb; ldw = D; K = 1024; scol = n0 + 4 * q4; W = a.w_out_b + (size_t)l * 1024 * D; WT = ws + WS_WOB + (size_t)l * D * 1024 * (MIX_F8 ? 1 : 2); if (MIX_F8) { d.f8 = 1; esz = 1; }
;                 if (BR_FUSE) { K = 1536; WT = ws + WS_WOA + (size_t)l * D * 1536; }
; template <unsigned MASK, bool ONE>
; __global__ void __launch_bounds__(NTHREADS, 2) fwd_kernel(Args a_unused) {
;     ...
;         if (IN(P + 1, 2)) { FRESH_TID();
;     ...
;             pg8::StaticOrderP S{T / 256, NP / 256, G, bx}; pg8::RowsContig AM; pg8::EpiProj E{proj, ropec, ropes, alow, pg8::W8_INV};
;             pg8::gemm_phase<pg8::EpiProj, pg8::StaticOrderP, pg8::RowsContig, true, true>(lds, tid, hbuf, (const bf16_t*)(ws + WS_WIN + (size_t)l * NP * D), 0, D / 2, S, AM, E);
.LBB0_265:
	s_or_b64 exec, exec, s[0:1]
	v_readlane_b32 s0, v253, 0
	v_readlane_b32 s1, v253, 1
	s_mov_b32 s2, s38
	s_waitcnt lgkmcnt(0)
	s_barrier
	s_nop 0
	v_mbcnt_lo_u32_b32 v0, s2, 0
	v_mbcnt_hi_u32_b32 v0, s2, v0
	v_readlane_b32 s2, v253, 7
	v_readlane_b32 s3, v253, 8
	v_add_u32_e32 v1, s78, v0
	s_andn2_b64 vcc, exec, s[2:3]
	v_readfirstlane_b32 s16, v1
	v_readlane_b32 s101, v255, 17
	s_movk_i32 s100, 0x100
	s_cmp_eq_u32 s101, 0
	s_cbranch_scc0 .Lpq_skip
	s_movk_i32 s100, 0xd8
	v_readlane_b32 s101, v253, 4
	s_nop 1
	s_cmp_lt_i32 s101, s100
	s_cbranch_scc1 .Lpq_skip
	s_mov_b32 s100, 0x7e80
	s_mov_b32 s101, 0xbe80
	v_writelane_b32 v251, s16, 0
	v_writelane_b32 v251, s17, 1
	v_writelane_b32 v251, s18, 2
	v_writelane_b32 v251, s19, 3
	v_writelane_b32 v251, s20, 4
	v_writelane_b32 v251, s21, 5
	v_writelane_b32 v251, s23, 6
	v_writelane_b32 v251, s25, 7
	v_writelane_b32 v251, s26, 8
	v_writelane_b32 v251, s33, 9
	v_writelane_b32 v251, s38, 10
	v_writelane_b32 v251, s39, 11
	v_writelane_b32 v251, s41, 12
	v_writelane_b32 v251, s42, 13
	v_writelane_b32 v251, s45, 14
	v_writelane_b32 v251, s48, 15
	v_writelane_b32 v251, s49, 16
	v_writelane_b32 v251, s50, 17
	v_writelane_b32 v251, s51, 18
	v_writelane_b32 v251, s74, 19
	v_writelane_b32 v251, s76, 20
	v_mov_b32_e32 v193, v3
	v_mov_b32_e32 v194, v33
	v_mov_b32_e32 v195, v59
	v_mov_b32_e32 v196, v63
	v_mov_b32_e32 v197, v110
	v_mov_b32_e32 v198, v111
	v_mov_b32_e32 v199, v114
	v_mov_b32_e32 v200, v115
	v_mov_b32_e32 v201, v149
	v_mov_b32_e32 v202, v153
	v_mov_b32_e32 v203, v157
	v_mov_b32_e32 v204, v161
	v_mov_b32_e32 v205, v165
	v_mov_b32_e32 v206, v169
	v_mov_b32_e32 v207, v173
	v_mov_b32_e32 v208, v177
	v_mov_b32_e32 v209, v178
	v_mov_b32_e32 v210, v179
	v_mov_b32_e32 v211, v180
	v_mov_b32_e32 v212, v181
	v_mov_b32_e32 v214, v182
	v_mov_b32_e32 v215, v183
	v_mov_b32_e32 v216, v184
	v_mov_b32_e32 v218, v185
	v_readlane_b32 s76, v253, 4
	v_readlane_b32 s8, v253, 0
	v_readlane_b32 s9, v253, 1
	s_nop 1
	s_sub_i32 s0, s76, 216
	s_lshr_b32 s1, s100, 3
	s_add_i32 s0, s0, s1
	s_lshr_b32 s33, s78, 6
	s_lshr_b32 s1, s0, 3
	s_lshl_b32 s1, s1, 6
	s_and_b32 s0, s0, 7
	s_lshl_b32 s0, s0, 2
	s_or_b32 s1, s1, s0
	s_and_b32 s0, s33, 3
	s_or_b32 s1, s1, s0
	s_lshr_b32 s0, s33, 2
	s_lshl_b32 s0, s0, 5
	s_or_b32 s1, s1, s0
	s_sub_i32 s100, s1, s33
	s_mov_b32 s76, 0
	s_movk_i32 s74, 40
	s_load_dwordx2 s[10:11], s[8:9], 0xa0
	v_mbcnt_lo_u32_b32 v69, -1, 0
	v_mbcnt_hi_u32_b32 v69, -1, v69
	s_mov_b64 exec, -1
	v_lshlrev_b32_e32 v76, 3, v69
	s_waitcnt lgkmcnt(0)
	s_lshl_b32 s47, s76, 3
	s_add_i32 s47, s47, s33
	s_add_i32 s47, s47, s100
	v_and_b32_e32 v2, 15, v69
	s_cmp_ge_i32 s47, s101
	v_ashrrev_i32_e32 v133, 4, v69
	s_cbranch_scc1 .LBB0_36_hq
	s_sub_i32 s1, 0xfcff, s47
	s_mul_hi_u32 s0, s1, 0x81848da9
	s_lshr_b32 s0, s0, 14
	s_mul_i32 s2, s0, 0x7e80
	s_sub_i32 s17, s1, s2
	s_cmpk_gt_u32 s17, 0x177f
	s_cbranch_scc0 .LBB0_37_hq
	s_cmpk_gt_u32 s17, 0x187f
	s_cbranch_scc0 .LBB0_39_hq
	s_cmpk_gt_u32 s17, 0x1a7f
	s_cbranch_scc0 .LBB0_40_hq
	s_cmpk_gt_u32 s17, 0x1e7f
	s_cbranch_scc0 .LBB0_41_hq
	s_lshl_b32 s1, s17, 6
	s_cmpk_gt_u32 s17, 0x5e7f
	s_cbranch_scc0 .LBB0_42_hq
	s_add_i32 s2, s17, 0xffffa180
	s_lshr_b32 s4, s2, 9
	s_lshl_b32 s2, s2, 1
	s_and_b32 s18, s2, 0x3c0
	s_load_dwordx2 s[2:3], s[8:9], 0x88
	s_lshl_b32 s5, s0, 4
	s_add_i32 s6, s4, s5
	s_mov_b32 s7, 0
	s_and_b32 s16, s1, 0x7c0
	s_lshl_b64 s[4:5], s[6:7], 23
	s_waitcnt lgkmcnt(0)
	s_add_u32 s4, s2, s4
	s_addc_u32 s5, s3, s5
	s_lshl_b64 s[2:3], s[6:7], 21
	s_add_u32 s2, s10, s2
	s_addc_u32 s3, s11, s3
	s_add_u32 s6, s2, 0x18600000
	v_lshl_or_b32 v0, v2, 2, s16
	s_addc_u32 s7, s3, 0
	s_mov_b64 s[2:3], 0
	s_branch .LBB0_43_hq
